# speedup vs baseline: 1.0025x; 1.0025x over previous
.LBB7_10:
	v_mbcnt_lo_u32_b32 v250, -1, 0
	v_mbcnt_hi_u32_b32 v250, -1, v250
	v_lshrrev_b32_e32 v250, 4, v250
	v_lshlrev_b32_e32 v250, 4, v250
	v_sub_u32_e32 v250, 0, v250
	v_ashrrev_i32_e32 v251, 31, v250
	s_cmp_lt_i32 s52, s25
	s_cselect_b64 s[4:5], -1, 0
	s_and_b64 vcc, s[50:51], s[4:5]
	v_mov_b32_e32 v164, s59
	v_mov_b32_e32 v165, s26
	s_and_b64 s[4:5], s[50:51], exec
	v_cndmask_b32_e32 v164, v164, v165, vcc
	s_cselect_b32 s4, s21, s35
	s_cselect_b32 s5, s20, s34
	v_lshl_add_u32 v165, s72, 8, v168
	v_mov_b32_e32 v186, s5
	v_mov_b32_e32 v187, s4
	s_cselect_b32 s4, s24, s27
	s_waitcnt vmcnt(0)
	v_pk_fma_f32 v[128:129], v[164:165], v[128:129], v[136:137] op_sel_hi:[0,1,1]
	v_pk_fma_f32 v[126:127], v[164:165], v[126:127], v[134:135] op_sel_hi:[0,1,1]
	v_pk_fma_f32 v[124:125], v[164:165], v[124:125], v[132:133] op_sel_hi:[0,1,1]
	v_pk_fma_f32 v[122:123], v[164:165], v[122:123], v[130:131] op_sel_hi:[0,1,1]
	v_lshl_add_u64 v[166:167], v[166:167], 1, v[186:187]
	v_mad_i64_i32 v[186:187], s[50:51], v165, s4, 0
	v_max_f32_e32 v126, 0, v126
	v_max_f32_e32 v188, 0, v122
	v_max_f32_e32 v122, 0, v127
	v_max_f32_e32 v127, 0, v123
	v_max_f32_e32 v123, 0, v128
	v_max_f32_e32 v128, 0, v124
	v_max_f32_e32 v124, 0, v129
	v_max_f32_e32 v125, 0, v125
	v_lshl_add_u64 v[186:187], v[186:187], 1, v[166:167]
	v_cvt_pk_f16_f32 v122, v126, v122
	v_cvt_pk_f16_f32 v123, v123, v124
	v_cvt_pk_f16_f32 v124, v188, v127
	v_cvt_pk_f16_f32 v125, v128, v125
	v_pk_fma_f32 v[120:121], v[164:165], v[120:121], v[144:145] op_sel_hi:[0,1,1]
	v_pk_fma_f32 v[118:119], v[164:165], v[118:119], v[142:143] op_sel_hi:[0,1,1]
	v_pk_fma_f32 v[116:117], v[164:165], v[116:117], v[140:141] op_sel_hi:[0,1,1]
	v_pk_fma_f32 v[114:115], v[164:165], v[114:115], v[138:139] op_sel_hi:[0,1,1]
	v_mov_b32_e32 v244, v122
	v_mov_b32_e32 v245, v123
	v_mov_b32_e32 v246, v124
	v_mov_b32_e32 v247, v125
	v_max_f32_e32 v118, 0, v118
	v_max_f32_e32 v117, 0, v117
	v_max_f32_e32 v122, 0, v114
	v_max_f32_e32 v114, 0, v119
	v_max_f32_e32 v119, 0, v115
	v_max_f32_e32 v115, 0, v120
	v_max_f32_e32 v120, 0, v116
	v_max_f32_e32 v116, 0, v121
	v_cvt_pk_f16_f32 v114, v118, v114
	v_cvt_pk_f16_f32 v115, v115, v116
	v_cvt_pk_f16_f32 v116, v122, v119
	v_cvt_pk_f16_f32 v117, v120, v117
	s_nop 1
	v_permlane16_swap_b32_e32 v244, v114
	v_permlane16_swap_b32_e32 v245, v115
	v_permlane16_swap_b32_e32 v246, v116
	v_permlane16_swap_b32_e32 v247, v117
	v_permlane32_swap_b32_e32 v244, v114
	v_permlane32_swap_b32_e32 v245, v115
	v_permlane32_swap_b32_e32 v246, v116
	v_permlane32_swap_b32_e32 v247, v117
	v_lshl_add_u64 v[252:253], v[186:187], 0, v[250:251]
	global_store_dwordx4 v[252:253], v[244:247], off
	global_store_dwordx4 v[252:253], v[114:117], off offset:64
	v_pk_fma_f32 v[112:113], v[164:165], v[112:113], v[136:137] op_sel_hi:[0,1,1]
	v_pk_fma_f32 v[110:111], v[164:165], v[110:111], v[134:135] op_sel_hi:[0,1,1]
	v_or_b32_e32 v114, 16, v165
	v_pk_fma_f32 v[108:109], v[164:165], v[108:109], v[132:133] op_sel_hi:[0,1,1]
	v_pk_fma_f32 v[106:107], v[164:165], v[106:107], v[130:131] op_sel_hi:[0,1,1]
	v_mad_i64_i32 v[114:115], s[50:51], v114, s4, 0
	v_max_f32_e32 v110, 0, v110
	v_max_f32_e32 v116, 0, v106
	v_max_f32_e32 v106, 0, v111
	v_max_f32_e32 v111, 0, v107
	v_max_f32_e32 v107, 0, v112
	v_max_f32_e32 v112, 0, v108
	v_max_f32_e32 v108, 0, v113
	v_max_f32_e32 v109, 0, v109
	v_lshl_add_u64 v[114:115], v[114:115], 1, v[166:167]
	v_cvt_pk_f16_f32 v106, v110, v106
	v_cvt_pk_f16_f32 v107, v107, v108
	v_cvt_pk_f16_f32 v108, v116, v111
	v_cvt_pk_f16_f32 v109, v112, v109
	v_pk_fma_f32 v[104:105], v[164:165], v[104:105], v[144:145] op_sel_hi:[0,1,1]
	v_pk_fma_f32 v[102:103], v[164:165], v[102:103], v[142:143] op_sel_hi:[0,1,1]
	v_pk_fma_f32 v[100:101], v[164:165], v[100:101], v[140:141] op_sel_hi:[0,1,1]
	v_pk_fma_f32 v[98:99], v[164:165], v[98:99], v[138:139] op_sel_hi:[0,1,1]
	v_mov_b32_e32 v244, v106
	v_mov_b32_e32 v245, v107
	v_mov_b32_e32 v246, v108
	v_mov_b32_e32 v247, v109
	v_max_f32_e32 v102, 0, v102
	v_max_f32_e32 v101, 0, v101
	v_max_f32_e32 v106, 0, v98
	v_max_f32_e32 v98, 0, v103
	v_max_f32_e32 v103, 0, v99
	v_max_f32_e32 v99, 0, v104
	v_max_f32_e32 v104, 0, v100
	v_max_f32_e32 v100, 0, v105
	v_cvt_pk_f16_f32 v98, v102, v98
	v_cvt_pk_f16_f32 v99, v99, v100
	v_cvt_pk_f16_f32 v100, v106, v103
	v_cvt_pk_f16_f32 v101, v104, v101
	s_nop 1
	v_permlane16_swap_b32_e32 v244, v98
	v_permlane16_swap_b32_e32 v245, v99
	v_permlane16_swap_b32_e32 v246, v100
	v_permlane16_swap_b32_e32 v247, v101
	v_permlane32_swap_b32_e32 v244, v98
	v_permlane32_swap_b32_e32 v245, v99
	v_permlane32_swap_b32_e32 v246, v100
	v_permlane32_swap_b32_e32 v247, v101
	v_lshl_add_u64 v[252:253], v[114:115], 0, v[250:251]
	global_store_dwordx4 v[252:253], v[244:247], off
	global_store_dwordx4 v[252:253], v[98:101], off offset:64
	v_pk_fma_f32 v[96:97], v[164:165], v[96:97], v[136:137] op_sel_hi:[0,1,1]
	v_pk_fma_f32 v[94:95], v[164:165], v[94:95], v[134:135] op_sel_hi:[0,1,1]
	v_or_b32_e32 v98, 32, v165
	v_pk_fma_f32 v[92:93], v[164:165], v[92:93], v[132:133] op_sel_hi:[0,1,1]
	v_pk_fma_f32 v[90:91], v[164:165], v[90:91], v[130:131] op_sel_hi:[0,1,1]
	v_mad_i64_i32 v[98:99], s[50:51], v98, s4, 0
	v_max_f32_e32 v94, 0, v94
	v_max_f32_e32 v100, 0, v90
	v_max_f32_e32 v90, 0, v95
	v_max_f32_e32 v95, 0, v91
	v_max_f32_e32 v91, 0, v96
	v_max_f32_e32 v96, 0, v92
	v_max_f32_e32 v92, 0, v97
	v_max_f32_e32 v93, 0, v93
	v_lshl_add_u64 v[98:99], v[98:99], 1, v[166:167]
	v_cvt_pk_f16_f32 v90, v94, v90
	v_cvt_pk_f16_f32 v91, v91, v92
	v_cvt_pk_f16_f32 v92, v100, v95
	v_cvt_pk_f16_f32 v93, v96, v93
	v_pk_fma_f32 v[88:89], v[164:165], v[88:89], v[144:145] op_sel_hi:[0,1,1]
	v_pk_fma_f32 v[86:87], v[164:165], v[86:87], v[142:143] op_sel_hi:[0,1,1]
	v_pk_fma_f32 v[84:85], v[164:165], v[84:85], v[140:141] op_sel_hi:[0,1,1]
	v_pk_fma_f32 v[82:83], v[164:165], v[82:83], v[138:139] op_sel_hi:[0,1,1]
	v_mov_b32_e32 v244, v90
	v_mov_b32_e32 v245, v91
	v_mov_b32_e32 v246, v92
	v_mov_b32_e32 v247, v93
	v_max_f32_e32 v86, 0, v86
	v_max_f32_e32 v85, 0, v85
	v_max_f32_e32 v90, 0, v82
	v_max_f32_e32 v82, 0, v87
	v_max_f32_e32 v87, 0, v83
	v_max_f32_e32 v83, 0, v88
	v_max_f32_e32 v88, 0, v84
	v_max_f32_e32 v84, 0, v89
	v_cvt_pk_f16_f32 v82, v86, v82
	v_cvt_pk_f16_f32 v83, v83, v84
	v_cvt_pk_f16_f32 v84, v90, v87
	v_cvt_pk_f16_f32 v85, v88, v85
	s_nop 1
	v_permlane16_swap_b32_e32 v244, v82
	v_permlane16_swap_b32_e32 v245, v83
	v_permlane16_swap_b32_e32 v246, v84
	v_permlane16_swap_b32_e32 v247, v85
	v_permlane32_swap_b32_e32 v244, v82
	v_permlane32_swap_b32_e32 v245, v83
	v_permlane32_swap_b32_e32 v246, v84
	v_permlane32_swap_b32_e32 v247, v85
	v_lshl_add_u64 v[252:253], v[98:99], 0, v[250:251]
	global_store_dwordx4 v[252:253], v[244:247], off
	global_store_dwordx4 v[252:253], v[82:85], off offset:64
	v_pk_fma_f32 v[80:81], v[164:165], v[80:81], v[136:137] op_sel_hi:[0,1,1]
	v_pk_fma_f32 v[78:79], v[164:165], v[78:79], v[134:135] op_sel_hi:[0,1,1]
	v_or_b32_e32 v82, 48, v165
	v_pk_fma_f32 v[76:77], v[164:165], v[76:77], v[132:133] op_sel_hi:[0,1,1]
	v_pk_fma_f32 v[74:75], v[164:165], v[74:75], v[130:131] op_sel_hi:[0,1,1]
	v_mad_i64_i32 v[82:83], s[50:51], v82, s4, 0
	v_max_f32_e32 v78, 0, v78
	v_max_f32_e32 v84, 0, v74
	v_max_f32_e32 v74, 0, v79
	v_max_f32_e32 v79, 0, v75
	v_max_f32_e32 v75, 0, v80
	v_max_f32_e32 v80, 0, v76
	v_max_f32_e32 v76, 0, v81
	v_max_f32_e32 v77, 0, v77
	v_lshl_add_u64 v[82:83], v[82:83], 1, v[166:167]
	v_cvt_pk_f16_f32 v74, v78, v74
	v_cvt_pk_f16_f32 v75, v75, v76
	v_cvt_pk_f16_f32 v76, v84, v79
	v_cvt_pk_f16_f32 v77, v80, v77
	v_pk_fma_f32 v[72:73], v[164:165], v[72:73], v[144:145] op_sel_hi:[0,1,1]
	v_pk_fma_f32 v[70:71], v[164:165], v[70:71], v[142:143] op_sel_hi:[0,1,1]
	v_pk_fma_f32 v[68:69], v[164:165], v[68:69], v[140:141] op_sel_hi:[0,1,1]
	v_pk_fma_f32 v[66:67], v[164:165], v[66:67], v[138:139] op_sel_hi:[0,1,1]
	v_mov_b32_e32 v244, v74
	v_mov_b32_e32 v245, v75
	v_mov_b32_e32 v246, v76
	v_mov_b32_e32 v247, v77
	v_max_f32_e32 v70, 0, v70
	v_max_f32_e32 v69, 0, v69
	v_max_f32_e32 v74, 0, v66
	v_max_f32_e32 v66, 0, v71
	v_max_f32_e32 v71, 0, v67
	v_max_f32_e32 v67, 0, v72
	v_max_f32_e32 v72, 0, v68
	v_max_f32_e32 v68, 0, v73
	v_cvt_pk_f16_f32 v66, v70, v66
	v_cvt_pk_f16_f32 v67, v67, v68
	v_cvt_pk_f16_f32 v68, v74, v71
	v_cvt_pk_f16_f32 v69, v72, v69
	s_nop 1
	v_permlane16_swap_b32_e32 v244, v66
	v_permlane16_swap_b32_e32 v245, v67
	v_permlane16_swap_b32_e32 v246, v68
	v_permlane16_swap_b32_e32 v247, v69
	v_permlane32_swap_b32_e32 v244, v66
	v_permlane32_swap_b32_e32 v245, v67
	v_permlane32_swap_b32_e32 v246, v68
	v_permlane32_swap_b32_e32 v247, v69
	v_lshl_add_u64 v[252:253], v[82:83], 0, v[250:251]
	global_store_dwordx4 v[252:253], v[244:247], off
	global_store_dwordx4 v[252:253], v[66:69], off offset:64
	v_pk_fma_f32 v[64:65], v[164:165], v[64:65], v[136:137] op_sel_hi:[0,1,1]
	v_pk_fma_f32 v[62:63], v[164:165], v[62:63], v[134:135] op_sel_hi:[0,1,1]
	v_add_u32_e32 v66, 0x80, v165
	v_pk_fma_f32 v[60:61], v[164:165], v[60:61], v[132:133] op_sel_hi:[0,1,1]
	v_pk_fma_f32 v[58:59], v[164:165], v[58:59], v[130:131] op_sel_hi:[0,1,1]
	v_mad_i64_i32 v[66:67], s[50:51], v66, s4, 0
	v_max_f32_e32 v62, 0, v62
	v_max_f32_e32 v68, 0, v58
	v_max_f32_e32 v58, 0, v63
	v_max_f32_e32 v63, 0, v59
	v_max_f32_e32 v59, 0, v64
	v_max_f32_e32 v64, 0, v60
	v_max_f32_e32 v60, 0, v65
	v_max_f32_e32 v61, 0, v61
	v_lshl_add_u64 v[66:67], v[66:67], 1, v[166:167]
	v_cvt_pk_f16_f32 v58, v62, v58
	v_cvt_pk_f16_f32 v59, v59, v60
	v_cvt_pk_f16_f32 v60, v68, v63
	v_cvt_pk_f16_f32 v61, v64, v61
	v_pk_fma_f32 v[56:57], v[164:165], v[56:57], v[144:145] op_sel_hi:[0,1,1]
	v_pk_fma_f32 v[54:55], v[164:165], v[54:55], v[142:143] op_sel_hi:[0,1,1]
	v_pk_fma_f32 v[52:53], v[164:165], v[52:53], v[140:141] op_sel_hi:[0,1,1]
	v_pk_fma_f32 v[50:51], v[164:165], v[50:51], v[138:139] op_sel_hi:[0,1,1]
	v_mov_b32_e32 v244, v58
	v_mov_b32_e32 v245, v59
	v_mov_b32_e32 v246, v60
	v_mov_b32_e32 v247, v61
	v_max_f32_e32 v54, 0, v54
	v_max_f32_e32 v53, 0, v53
	v_max_f32_e32 v58, 0, v50
	v_max_f32_e32 v50, 0, v55
	v_max_f32_e32 v55, 0, v51
	v_max_f32_e32 v51, 0, v56
	v_max_f32_e32 v56, 0, v52
	v_max_f32_e32 v52, 0, v57
	v_cvt_pk_f16_f32 v50, v54, v50
	v_cvt_pk_f16_f32 v51, v51, v52
	v_cvt_pk_f16_f32 v52, v58, v55
	v_cvt_pk_f16_f32 v53, v56, v53
	s_nop 1
	v_permlane16_swap_b32_e32 v244, v50
	v_permlane16_swap_b32_e32 v245, v51
	v_permlane16_swap_b32_e32 v246, v52
	v_permlane16_swap_b32_e32 v247, v53
	v_permlane32_swap_b32_e32 v244, v50
	v_permlane32_swap_b32_e32 v245, v51
	v_permlane32_swap_b32_e32 v246, v52
	v_permlane32_swap_b32_e32 v247, v53
	v_lshl_add_u64 v[252:253], v[66:67], 0, v[250:251]
	global_store_dwordx4 v[252:253], v[244:247], off
	global_store_dwordx4 v[252:253], v[50:53], off offset:64
	v_pk_fma_f32 v[48:49], v[164:165], v[48:49], v[136:137] op_sel_hi:[0,1,1]
	v_pk_fma_f32 v[46:47], v[164:165], v[46:47], v[134:135] op_sel_hi:[0,1,1]
	v_add_u32_e32 v50, 0x90, v165
	v_pk_fma_f32 v[44:45], v[164:165], v[44:45], v[132:133] op_sel_hi:[0,1,1]
	v_pk_fma_f32 v[42:43], v[164:165], v[42:43], v[130:131] op_sel_hi:[0,1,1]
	v_mad_i64_i32 v[50:51], s[50:51], v50, s4, 0
	v_max_f32_e32 v46, 0, v46
	v_max_f32_e32 v52, 0, v42
	v_max_f32_e32 v42, 0, v47
	v_max_f32_e32 v47, 0, v43
	v_max_f32_e32 v43, 0, v48
	v_max_f32_e32 v48, 0, v44
	v_max_f32_e32 v44, 0, v49
	v_max_f32_e32 v45, 0, v45
	v_lshl_add_u64 v[50:51], v[50:51], 1, v[166:167]
	v_cvt_pk_f16_f32 v42, v46, v42
	v_cvt_pk_f16_f32 v43, v43, v44
	v_cvt_pk_f16_f32 v44, v52, v47
	v_cvt_pk_f16_f32 v45, v48, v45
	v_pk_fma_f32 v[40:41], v[164:165], v[40:41], v[144:145] op_sel_hi:[0,1,1]
	v_pk_fma_f32 v[38:39], v[164:165], v[38:39], v[142:143] op_sel_hi:[0,1,1]
	v_pk_fma_f32 v[36:37], v[164:165], v[36:37], v[140:141] op_sel_hi:[0,1,1]
	v_pk_fma_f32 v[34:35], v[164:165], v[34:35], v[138:139] op_sel_hi:[0,1,1]
	v_mov_b32_e32 v244, v42
	v_mov_b32_e32 v245, v43
	v_mov_b32_e32 v246, v44
	v_mov_b32_e32 v247, v45
	v_max_f32_e32 v38, 0, v38
	v_max_f32_e32 v37, 0, v37
	v_max_f32_e32 v42, 0, v34
	v_max_f32_e32 v34, 0, v39
	v_max_f32_e32 v39, 0, v35
	v_max_f32_e32 v35, 0, v40
	v_max_f32_e32 v40, 0, v36
	v_max_f32_e32 v36, 0, v41
	v_cvt_pk_f16_f32 v34, v38, v34
	v_cvt_pk_f16_f32 v35, v35, v36
	v_cvt_pk_f16_f32 v36, v42, v39
	v_cvt_pk_f16_f32 v37, v40, v37
	s_nop 1
	v_permlane16_swap_b32_e32 v244, v34
	v_permlane16_swap_b32_e32 v245, v35
	v_permlane16_swap_b32_e32 v246, v36
	v_permlane16_swap_b32_e32 v247, v37
	v_permlane32_swap_b32_e32 v244, v34
	v_permlane32_swap_b32_e32 v245, v35
	v_permlane32_swap_b32_e32 v246, v36
	v_permlane32_swap_b32_e32 v247, v37
	v_lshl_add_u64 v[252:253], v[50:51], 0, v[250:251]
	global_store_dwordx4 v[252:253], v[244:247], off
	global_store_dwordx4 v[252:253], v[34:37], off offset:64
	v_pk_fma_f32 v[32:33], v[164:165], v[32:33], v[136:137] op_sel_hi:[0,1,1]
	v_pk_fma_f32 v[30:31], v[164:165], v[30:31], v[134:135] op_sel_hi:[0,1,1]
	v_add_u32_e32 v34, 0xa0, v165
	v_pk_fma_f32 v[28:29], v[164:165], v[28:29], v[132:133] op_sel_hi:[0,1,1]
	v_pk_fma_f32 v[26:27], v[164:165], v[26:27], v[130:131] op_sel_hi:[0,1,1]
	v_mad_i64_i32 v[34:35], s[50:51], v34, s4, 0
	v_max_f32_e32 v30, 0, v30
	v_max_f32_e32 v36, 0, v26
	v_max_f32_e32 v26, 0, v31
	v_max_f32_e32 v31, 0, v27
	v_max_f32_e32 v27, 0, v32
	v_max_f32_e32 v32, 0, v28
	v_max_f32_e32 v28, 0, v33
	v_max_f32_e32 v29, 0, v29
	v_lshl_add_u64 v[34:35], v[34:35], 1, v[166:167]
	v_cvt_pk_f16_f32 v26, v30, v26
	v_cvt_pk_f16_f32 v27, v27, v28
	v_cvt_pk_f16_f32 v28, v36, v31
	v_cvt_pk_f16_f32 v29, v32, v29
	v_pk_fma_f32 v[24:25], v[164:165], v[24:25], v[144:145] op_sel_hi:[0,1,1]
	v_pk_fma_f32 v[22:23], v[164:165], v[22:23], v[142:143] op_sel_hi:[0,1,1]
	v_pk_fma_f32 v[20:21], v[164:165], v[20:21], v[140:141] op_sel_hi:[0,1,1]
	v_pk_fma_f32 v[18:19], v[164:165], v[18:19], v[138:139] op_sel_hi:[0,1,1]
	v_mov_b32_e32 v244, v26
	v_mov_b32_e32 v245, v27
	v_mov_b32_e32 v246, v28
	v_mov_b32_e32 v247, v29
	v_max_f32_e32 v22, 0, v22
	v_max_f32_e32 v21, 0, v21
	v_max_f32_e32 v26, 0, v18
	v_max_f32_e32 v18, 0, v23
	v_max_f32_e32 v23, 0, v19
	v_max_f32_e32 v19, 0, v24
	v_max_f32_e32 v24, 0, v20
	v_max_f32_e32 v20, 0, v25
	v_cvt_pk_f16_f32 v18, v22, v18
	v_cvt_pk_f16_f32 v19, v19, v20
	v_cvt_pk_f16_f32 v20, v26, v23
	v_cvt_pk_f16_f32 v21, v24, v21
	s_nop 1
	v_permlane16_swap_b32_e32 v244, v18
	v_permlane16_swap_b32_e32 v245, v19
	v_permlane16_swap_b32_e32 v246, v20
	v_permlane16_swap_b32_e32 v247, v21
	v_permlane32_swap_b32_e32 v244, v18
	v_permlane32_swap_b32_e32 v245, v19
	v_permlane32_swap_b32_e32 v246, v20
	v_permlane32_swap_b32_e32 v247, v21
	v_lshl_add_u64 v[252:253], v[34:35], 0, v[250:251]
	global_store_dwordx4 v[252:253], v[244:247], off
	global_store_dwordx4 v[252:253], v[18:21], off offset:64
	v_pk_fma_f32 v[16:17], v[164:165], v[16:17], v[136:137] op_sel_hi:[0,1,1]
	v_pk_fma_f32 v[14:15], v[164:165], v[14:15], v[134:135] op_sel_hi:[0,1,1]
	v_add_u32_e32 v18, 0xb0, v165
	v_pk_fma_f32 v[12:13], v[164:165], v[12:13], v[132:133] op_sel_hi:[0,1,1]
	v_pk_fma_f32 v[10:11], v[164:165], v[10:11], v[130:131] op_sel_hi:[0,1,1]
	v_mad_i64_i32 v[18:19], s[4:5], v18, s4, 0
	v_max_f32_e32 v14, 0, v14
	v_max_f32_e32 v20, 0, v10
	v_max_f32_e32 v10, 0, v15
	v_max_f32_e32 v15, 0, v11
	v_max_f32_e32 v11, 0, v16
	v_max_f32_e32 v16, 0, v12
	v_max_f32_e32 v12, 0, v17
	v_max_f32_e32 v13, 0, v13
	v_lshl_add_u64 v[18:19], v[18:19], 1, v[166:167]
	v_cvt_pk_f16_f32 v10, v14, v10
	v_cvt_pk_f16_f32 v11, v11, v12
	v_cvt_pk_f16_f32 v12, v20, v15
	v_cvt_pk_f16_f32 v13, v16, v13
	v_pk_fma_f32 v[8:9], v[164:165], v[8:9], v[144:145] op_sel_hi:[0,1,1]
	v_pk_fma_f32 v[6:7], v[164:165], v[6:7], v[142:143] op_sel_hi:[0,1,1]
	v_pk_fma_f32 v[4:5], v[164:165], v[4:5], v[140:141] op_sel_hi:[0,1,1]
	v_pk_fma_f32 v[2:3], v[164:165], v[2:3], v[138:139] op_sel_hi:[0,1,1]
	v_mov_b32_e32 v244, v10
	v_mov_b32_e32 v245, v11
	v_mov_b32_e32 v246, v12
	v_mov_b32_e32 v247, v13
	v_max_f32_e32 v6, 0, v6
	v_max_f32_e32 v5, 0, v5
	v_max_f32_e32 v10, 0, v2
	v_max_f32_e32 v2, 0, v7
	v_max_f32_e32 v7, 0, v3
	v_max_f32_e32 v3, 0, v8
	v_max_f32_e32 v8, 0, v4
	v_max_f32_e32 v4, 0, v9
	v_cvt_pk_f16_f32 v2, v6, v2
	v_cvt_pk_f16_f32 v3, v3, v4
	v_cvt_pk_f16_f32 v4, v10, v7
	v_cvt_pk_f16_f32 v5, v8, v5
	s_and_b64 vcc, exec, s[44:45]
	s_mov_b32 s74, s69
	s_mov_b32 s73, s71
	s_mov_b32 s72, s70
	s_mov_b64 s[50:51], s[48:49]
	s_mov_b64 s[4:5], s[46:47]
	s_nop 1
	v_permlane16_swap_b32_e32 v244, v2
	v_permlane16_swap_b32_e32 v245, v3
	v_permlane16_swap_b32_e32 v246, v4
	v_permlane16_swap_b32_e32 v247, v5
	v_permlane32_swap_b32_e32 v244, v2
	v_permlane32_swap_b32_e32 v245, v3
	v_permlane32_swap_b32_e32 v246, v4
	v_permlane32_swap_b32_e32 v247, v5
	v_lshl_add_u64 v[252:253], v[18:19], 0, v[250:251]
	global_store_dwordx4 v[252:253], v[244:247], off
	global_store_dwordx4 v[252:253], v[2:5], off offset:64
	s_cbranch_vccnz .LBB7_33

	.amdhsa_kernel _Z6k_gemmIN3pg84EpiHILi1ELb0EEELb0EEvNS0_4GemmET_6WtTailPj
		.amdhsa_group_segment_fixed_size 0
		.amdhsa_private_segment_fixed_size 0
		.amdhsa_kernarg_size 568
		.amdhsa_user_sgpr_count 2
		.amdhsa_user_sgpr_dispatch_ptr 0
		.amdhsa_user_sgpr_queue_ptr 0
		.amdhsa_user_sgpr_kernarg_segment_ptr 1
		.amdhsa_user_sgpr_dispatch_id 0
		.amdhsa_user_sgpr_kernarg_preload_length 0
		.amdhsa_user_sgpr_kernarg_preload_offset 0
		.amdhsa_user_sgpr_private_segment_size 0
		.amdhsa_uses_dynamic_stack 0
		.amdhsa_enable_private_segment 0
		.amdhsa_system_sgpr_workgroup_id_x 1
		.amdhsa_system_sgpr_workgroup_id_y 0
		.amdhsa_system_sgpr_workgroup_id_z 0
		.amdhsa_system_sgpr_workgroup_info 0
		.amdhsa_system_vgpr_workitem_id 0
		.amdhsa_next_free_vgpr 256
		.amdhsa_next_free_sgpr 79
		.amdhsa_accum_offset 256
		.amdhsa_reserve_vcc 1
		.amdhsa_float_round_mode_32 0
		.amdhsa_float_round_mode_16_64 0
		.amdhsa_float_denorm_mode_32 3
		.amdhsa_float_denorm_mode_16_64 3
		.amdhsa_dx10_clamp 1
		.amdhsa_ieee_mode 1
		.amdhsa_fp16_overflow 0
		.amdhsa_tg_split 0
		.amdhsa_exception_fp_ieee_invalid_op 0
		.amdhsa_exception_fp_denorm_src 0
		.amdhsa_exception_fp_ieee_div_zero 0
		.amdhsa_exception_fp_ieee_overflow 0
		.amdhsa_exception_fp_ieee_underflow 0
		.amdhsa_exception_fp_ieee_inexact 0
		.amdhsa_exception_int_div_zero 0
	.end_amdhsa_kernel

amdhsa.kernels:
  - .agpr_count:     0
    .args:
      - .offset:         0
        .size:           384
        .value_kind:     by_value
    .group_segment_fixed_size: 5120
    .kernarg_segment_align: 8
    .kernarg_segment_size: 384
    .language:       OpenCL C
    .language_version:
      - 2
      - 0
    .max_flat_workgroup_size: 256
    .name:           _Z6k_prep6WtArgs
    .private_segment_fixed_size: 0
    .sgpr_count:     38
    .sgpr_spill_count: 0
    .symbol:         _Z6k_prep6WtArgs.kd
    .uniform_work_group_size: 1
    .uses_dynamic_stack: false
    .vgpr_count:     29
    .vgpr_spill_count: 0
    .wavefront_size: 64
  - .agpr_count:     0
    .args:
      - .actual_access:  read_only
        .address_space:  global
        .offset:         0
        .size:           8
        .value_kind:     global_buffer
      - .actual_access:  read_only
        .address_space:  global
        .offset:         8
        .size:           8
        .value_kind:     global_buffer
      - .actual_access:  read_only
        .address_space:  global
        .offset:         16
        .size:           8
        .value_kind:     global_buffer
      - .actual_access:  write_only
        .address_space:  global
        .offset:         24
        .size:           8
        .value_kind:     global_buffer
      - .actual_access:  write_only
        .address_space:  global
        .offset:         32
        .size:           8
        .value_kind:     global_buffer
      - .actual_access:  write_only
        .address_space:  global
        .offset:         40
        .size:           8
        .value_kind:     global_buffer
      - .offset:         48
        .size:           4
        .value_kind:     by_value
    .group_segment_fixed_size: 0
    .kernarg_segment_align: 8
    .kernarg_segment_size: 52
    .language:       OpenCL C
    .language_version:
      - 2
      - 0
    .max_flat_workgroup_size: 256
    .name:           _Z4k_lnPKDF16_PKfS2_PfPDF16_Phi
    .private_segment_fixed_size: 0
    .sgpr_count:     18
    .sgpr_spill_count: 0
    .symbol:         _Z4k_lnPKDF16_PKfS2_PfPDF16_Phi.kd
    .uniform_work_group_size: 1
    .uses_dynamic_stack: false
    .vgpr_count:     59
    .vgpr_spill_count: 0
    .wavefront_size: 64
  - .agpr_count:     0
    .args:
      - .offset:         0
        .size:           56
        .value_kind:     by_value
      - .offset:         56
        .size:           72
        .value_kind:     by_value
      - .offset:         128
        .size:           176
        .value_kind:     by_value
      - .address_space:  global
        .offset:         304
        .size:           8
        .value_kind:     global_buffer
      - .offset:         312
        .size:           4
        .value_kind:     hidden_block_count_x
      - .offset:         316
        .size:           4
        .value_kind:     hidden_block_count_y
      - .offset:         320
        .size:           4
        .value_kind:     hidden_block_count_z
      - .offset:         324
        .size:           2
        .value_kind:     hidden_group_size_x
      - .offset:         326
        .size:           2
        .value_kind:     hidden_group_size_y
      - .offset:         328
        .size:           2
        .value_kind:     hidden_group_size_z
      - .offset:         330
        .size:           2
        .value_kind:     hidden_remainder_x
      - .offset:         332
        .size:           2
        .value_kind:     hidden_remainder_y
      - .offset:         334
        .size:           2
        .value_kind:     hidden_remainder_z
      - .offset:         352
        .size:           8
        .value_kind:     hidden_global_offset_x
      - .offset:         360
        .size:           8
        .value_kind:     hidden_global_offset_y
      - .offset:         368
        .size:           8
        .value_kind:     hidden_global_offset_z
      - .offset:         376
        .size:           2
        .value_kind:     hidden_grid_dims
      - .offset:         432
        .size:           4
        .value_kind:     hidden_dynamic_lds_size
    .group_segment_fixed_size: 0
    .kernarg_segment_align: 8
    .kernarg_segment_size: 568
    .language:       OpenCL C
    .language_version:
      - 2
      - 0
    .max_flat_workgroup_size: 512
    .name:           _Z6k_gemmIN3pg84EpiHILi0ELb1EEELb1EEvNS0_4GemmET_6WtTailPj
    .private_segment_fixed_size: 0
    .sgpr_count:     72
    .sgpr_spill_count: 5
    .symbol:         _Z6k_gemmIN3pg84EpiHILi0ELb1EEELb1EEvNS0_4GemmET_6WtTailPj.kd
    .uniform_work_group_size: 1
    .uses_dynamic_stack: false
    .vgpr_count:     240
    .vgpr_spill_count: 0
    .wavefront_size: 64
  - .agpr_count:     0
    .args:
      - .address_space:  global
        .offset:         0
        .size:           8
        .value_kind:     global_buffer
      - .address_space:  global
        .offset:         8
        .size:           8
        .value_kind:     global_buffer
      - .address_space:  global
        .offset:         16
        .size:           8
        .value_kind:     global_buffer
      - .address_space:  global
        .offset:         24
        .size:           8
        .value_kind:     global_buffer
      - .address_space:  global
        .offset:         32
        .size:           8
        .value_kind:     global_buffer
    .group_segment_fixed_size: 0
    .kernarg_segment_align: 8
    .kernarg_segment_size: 40
    .language:       OpenCL C
    .language_version:
      - 2
      - 0
    .max_flat_workgroup_size: 512
    .name:           _Z6k_attnILi1024ELi1024ELi1024ELi1024ELi3072ELi1024ELb1ELb1EEvPKDF16_S1_S1_PKfPDF16_
    .private_segment_fixed_size: 0
    .sgpr_count:     55
    .sgpr_spill_count: 0
    .symbol:         _Z6k_attnILi1024ELi1024ELi1024ELi1024ELi3072ELi1024ELb1ELb1EEvPKDF16_S1_S1_PKfPDF16_.kd
    .uniform_work_group_size: 1
    .uses_dynamic_stack: false
    .vgpr_count:     224
    .vgpr_spill_count: 0
    .wavefront_size: 64
  - .agpr_count:     0
    .args:
      - .address_space:  global
        .offset:         0
        .size:           8
        .value_kind:     global_buffer
      - .address_space:  global
        .offset:         8
        .size:           8
        .value_kind:     global_buffer
      - .offset:         16
        .size:           4
        .value_kind:     by_value
      - .offset:         20
        .size:           4
        .value_kind:     by_value
      - .offset:         24
        .size:           4
        .value_kind:     by_value
      - .offset:         32
        .size:           32
        .value_kind:     by_value
    .group_segment_fixed_size: 0
    .kernarg_segment_align: 8
    .kernarg_segment_size: 64
    .language:       OpenCL C
    .language_version:
      - 2
      - 0
    .max_flat_workgroup_size: 512
    .name:           _ZN2g811k_gemm128f8INS_6EpiResEEEvPKhS3_iiiT_
    .private_segment_fixed_size: 0
    .sgpr_count:     34
    .sgpr_spill_count: 0
    .symbol:         _ZN2g811k_gemm128f8INS_6EpiResEEEvPKhS3_iiiT_.kd
    .uniform_work_group_size: 1
    .uses_dynamic_stack: false
    .vgpr_count:     98
    .vgpr_spill_count: 0
    .wavefront_size: 64
  - .agpr_count:     0
    .args:
      - .address_space:  global
        .offset:         0
        .size:           8
        .value_kind:     global_buffer
      - .address_space:  global
        .offset:         8
        .size:           8
        .value_kind:     global_buffer
      - .offset:         16
        .size:           4
        .value_kind:     by_value
      - .offset:         20
        .size:           4
        .value_kind:     by_value
      - .offset:         24
        .size:           4
        .value_kind:     by_value
      - .offset:         32
        .size:           16
        .value_kind:     by_value
    .group_segment_fixed_size: 0
    .kernarg_segment_align: 8
    .kernarg_segment_size: 48
    .language:       OpenCL C
    .language_version:
      - 2
      - 0
    .max_flat_workgroup_size: 512
    .name:           _ZN2g811k_gemm128f8INS_5EpiQ8EEEvPKhS3_iiiT_
    .private_segment_fixed_size: 0
    .sgpr_count:     72
    .sgpr_spill_count: 0
    .symbol:         _ZN2g811k_gemm128f8INS_5EpiQ8EEEvPKhS3_iiiT_.kd
    .uniform_work_group_size: 1
    .uses_dynamic_stack: false
    .vgpr_count:     240
    .vgpr_spill_count: 0
    .wavefront_size: 64
  - .agpr_count:     0
    .args:
      - .address_space:  global
        .offset:         0
        .size:           8
        .value_kind:     global_buffer
      - .address_space:  global
        .offset:         8
        .size:           8
        .value_kind:     global_buffer
      - .address_space:  global
        .offset:         16
        .size:           8
        .value_kind:     global_buffer
      - .address_space:  global
        .offset:         24
        .size:           8
        .value_kind:     global_buffer
      - .address_space:  global
        .offset:         32
        .size:           8
        .value_kind:     global_buffer
    .group_segment_fixed_size: 0
    .kernarg_segment_align: 8
    .kernarg_segment_size: 40
    .language:       OpenCL C
    .language_version:
      - 2
      - 0
    .max_flat_workgroup_size: 512
    .name:           _Z6k_attnILi1024ELi2048ELi1024ELi1024ELi2048ELi1024ELb1ELb1EEvPKDF16_S1_S1_PKfPDF16_
    .private_segment_fixed_size: 0
    .sgpr_count:     52
    .sgpr_spill_count: 0
    .symbol:         _Z6k_attnILi1024ELi2048ELi1024ELi1024ELi2048ELi1024ELb1ELb1EEvPKDF16_S1_S1_PKfPDF16_.kd
    .uniform_work_group_size: 1
    .uses_dynamic_stack: false
    .vgpr_count:     224
    .vgpr_spill_count: 0
    .wavefront_size: 64
  - .agpr_count:     0
    .args:
      - .offset:         0
        .size:           56
        .value_kind:     by_value
      - .offset:         56
        .size:           72
        .value_kind:     by_value
      - .offset:         128
        .size:           176
        .value_kind:     by_value
      - .address_space:  global
        .offset:         304
        .size:           8
        .value_kind:     global_buffer
      - .offset:         312
        .size:           4
        .value_kind:     hidden_block_count_x
      - .offset:         316
        .size:           4
        .value_kind:     hidden_block_count_y
      - .offset:         320
        .size:           4
        .value_kind:     hidden_block_count_z
      - .offset:         324
        .size:           2
        .value_kind:     hidden_group_size_x
      - .offset:         326
        .size:           2
        .value_kind:     hidden_group_size_y
      - .offset:         328
        .size:           2
        .value_kind:     hidden_group_size_z
      - .offset:         330
        .size:           2
        .value_kind:     hidden_remainder_x
      - .offset:         332
        .size:           2
        .value_kind:     hidden_remainder_y
      - .offset:         334
        .size:           2
        .value_kind:     hidden_remainder_z
      - .offset:         352
        .size:           8
        .value_kind:     hidden_global_offset_x
      - .offset:         360
        .size:           8
        .value_kind:     hidden_global_offset_y
      - .offset:         368
        .size:           8
        .value_kind:     hidden_global_offset_z
      - .offset:         376
        .size:           2
        .value_kind:     hidden_grid_dims
      - .offset:         432
        .size:           4
        .value_kind:     hidden_dynamic_lds_size
    .group_segment_fixed_size: 0
    .kernarg_segment_align: 8
    .kernarg_segment_size: 568
    .language:       OpenCL C
    .language_version:
      - 2
      - 0
    .max_flat_workgroup_size: 512
    .name:           _Z6k_gemmIN3pg84EpiHILi1ELb0EEELb0EEvNS0_4GemmET_6WtTailPj
    .private_segment_fixed_size: 0
    .sgpr_count:     85
    .sgpr_spill_count: 0
    .symbol:         _Z6k_gemmIN3pg84EpiHILi1ELb0EEELb0EEvNS0_4GemmET_6WtTailPj.kd
    .uniform_work_group_size: 1
    .uses_dynamic_stack: false
    .vgpr_count:     256
    .vgpr_spill_count: 0
    .wavefront_size: 64
  - .agpr_count:     0
    .args:
      - .address_space:  global
        .offset:         0
        .size:           8
        .value_kind:     global_buffer
      - .address_space:  global
        .offset:         8
        .size:           8
        .value_kind:     global_buffer
      - .offset:         16
        .size:           4
        .value_kind:     by_value
      - .offset:         20
        .size:           4
        .value_kind:     by_value
      - .offset:         24
        .size:           4
        .value_kind:     by_value
      - .offset:         32
        .size:           32
        .value_kind:     by_value
    .group_segment_fixed_size: 0
    .kernarg_segment_align: 8
    .kernarg_segment_size: 64
    .language:       OpenCL C
    .language_version:
      - 2
      - 0
    .max_flat_workgroup_size: 512
    .name:           _ZN4g1289k_gemm128INS_8EpiRes16EEEvPKDF16_S3_iiiT_
    .private_segment_fixed_size: 0
    .sgpr_count:     35
    .sgpr_spill_count: 0
    .symbol:         _ZN4g1289k_gemm128INS_8EpiRes16EEEvPKDF16_S3_iiiT_.kd
    .uniform_work_group_size: 1
    .uses_dynamic_stack: false
    .vgpr_count:     112
    .vgpr_spill_count: 0
    .wavefront_size: 64
